# L1 W_in RoPE epilogue: rope-table rows of groups 1..5 loaded at epilogue start into dead regs, per-group loads replaced by v_mov copies
# speedup vs baseline: 1.0070x; 1.0070x over previous
; #define GAS __attribute__((address_space(1)))
; __device__ __forceinline__ unsigned cvt_pk_bf16(float lo, float hi) { unsigned r; asm volatile("v_cvt_pk_bf16_f32 %0, %1, %2" : "=v"(r) : "v"(lo), "v"(hi)); return r; }
;     __device__ __forceinline__ bool operator()(f32x4 (&acc)[2][2][4][2], const Unit& u, int wr, int wc, int fr, int fq, LAS unsigned char* scr) const {
;     ...
;         if (mode >= 4) {
;             const float sc = (mode == 4) ? 0.08838834764831845f : 1.0f;
;             const int i0 = 16 * wc + 4 * fq;
; #pragma unroll
;             for (int ai = 0; ai < 2; ++ai)
; #pragma unroll
;                 for (int m = 0; m < 4; ++m) { const int row = row0 + ai * 128 + m * 16; GAS bf16_t* rowp = H + HOFF(colt, row) + cl;
;                     const f32x4 cs0 = rope[(size_t)row * 32 + (i0 >> 1)], cs1 = rope[(size_t)row * 32 + (i0 >> 1) + 1];
; #pragma unroll
;                     for (int bj = 0; bj < 2; ++bj) { const f32x4 v0 = acc[ai][bj][m][0], v1 = acc[ai][bj][m][1]; u32x4 w;
;                         w.x = cvt_pk_bf16((v0[0] * cs0[0] - v0[1] * cs0[1]) * sc, (v0[1] * cs0[0] + v0[0] * cs0[1]) * sc);
;                         w.y = cvt_pk_bf16((v0[2] * cs0[2] - v0[3] * cs0[3]) * sc, (v0[3] * cs0[2] + v0[2] * cs0[3]) * sc);
;                         w.z = cvt_pk_bf16((v1[0] * cs1[0] - v1[1] * cs1[1]) * sc, (v1[1] * cs1[0] + v1[0] * cs1[1]) * sc);
;                         w.w = cvt_pk_bf16((v1[2] * cs1[2] - v1[3] * cs1[3]) * sc, (v1[3] * cs1[2] + v1[2] * cs1[3]) * sc);
;                         *(GAS u32x4*)(rowp + (size_t)bj * T * 128) = w; } }
;             return false;
.LBB0_2230:
	s_and_b64 vcc, exec, s[8:9]
	s_cbranch_vccz .LBB0_2232
	v_lshlrev_b64 v[4:5], 9, v[18:19]
	v_lshl_add_u64 v[8:9], v[178:179], 0, v[4:5]
	s_mov_b64 s[98:99], 0x2000
	s_mov_b64 s[100:101], 0x10000
	v_lshl_add_u64 v[196:197], v[8:9], 0, s[98:99]
	v_lshl_add_u64 v[216:217], v[196:197], 0, s[98:99]
	v_lshl_add_u64 v[224:225], v[216:217], 0, s[98:99]
	v_lshl_add_u64 v[232:233], v[8:9], 0, s[100:101]
	v_lshl_add_u64 v[240:241], v[232:233], 0, s[98:99]
	global_load_dwordx4 v[190:193], v[196:197], off
	global_load_dwordx4 v[194:197], v[196:197], off offset:16
	global_load_dwordx4 v[210:213], v[216:217], off
	global_load_dwordx4 v[214:217], v[216:217], off offset:16
	global_load_dwordx4 v[218:221], v[224:225], off
	global_load_dwordx4 v[222:225], v[224:225], off offset:16
	global_load_dwordx4 v[226:229], v[232:233], off
	global_load_dwordx4 v[230:233], v[232:233], off offset:16
	global_load_dwordx4 v[234:237], v[240:241], off
	global_load_dwordx4 v[238:241], v[240:241], off offset:16
	global_load_dwordx4 v[4:7], v[8:9], off
	s_nop 0
	global_load_dwordx4 v[8:11], v[8:9], off offset:16
	v_add_u32_e32 v14, 16, v18
	v_add_co_u32_e32 v12, vcc, s77, v2
	v_ashrrev_i32_e32 v15, 31, v14
	s_nop 0
	v_addc_co_u32_e32 v13, vcc, 0, v3, vcc
	v_lshlrev_b64 v[16:17], 9, v[14:15]
	v_lshl_add_u64 v[16:17], v[178:179], 0, v[16:17]
	s_waitcnt vmcnt(0)
	v_pk_mul_f32 v[20:21], v[160:161], v[6:7]
	v_pk_mul_f32 v[22:23], v[158:159], v[4:5]
	v_pk_mul_f32 v[24:25], v[158:159], v[4:5] op_sel:[1,0] op_sel_hi:[0,1]
	v_pk_mul_f32 v[26:27], v[160:161], v[6:7] op_sel:[1,0] op_sel_hi:[0,1]
	v_pk_mul_f32 v[28:29], v[156:157], v[10:11]
	v_pk_mul_f32 v[30:31], v[154:155], v[8:9]
	v_pk_mul_f32 v[32:33], v[154:155], v[8:9] op_sel:[1,0] op_sel_hi:[0,1]
	v_pk_mul_f32 v[154:155], v[156:157], v[10:11] op_sel:[1,0] op_sel_hi:[0,1]
	v_pk_mul_f32 v[156:157], v[152:153], v[6:7]
	v_pk_mul_f32 v[158:159], v[150:151], v[4:5]
	v_pk_mul_f32 v[4:5], v[150:151], v[4:5] op_sel:[1,0] op_sel_hi:[0,1]
	v_pk_mul_f32 v[6:7], v[152:153], v[6:7] op_sel:[1,0] op_sel_hi:[0,1]
	v_pk_mul_f32 v[150:151], v[148:149], v[10:11]
	v_pk_mul_f32 v[152:153], v[146:147], v[8:9]
	v_pk_mul_f32 v[8:9], v[146:147], v[8:9] op_sel:[1,0] op_sel_hi:[0,1]
	v_pk_mul_f32 v[10:11], v[148:149], v[10:11] op_sel:[1,0] op_sel_hi:[0,1]
	v_sub_f32_e32 v19, v22, v23
	v_add_f32_e32 v22, v24, v25
	v_sub_f32_e32 v20, v20, v21
	v_add_f32_e32 v21, v26, v27
	v_sub_f32_e32 v23, v30, v31
	v_add_f32_e32 v24, v32, v33
	v_sub_f32_e32 v25, v28, v29
	v_add_f32_e32 v26, v154, v155
	v_sub_f32_e32 v27, v158, v159
	v_add_f32_e32 v4, v4, v5
	v_sub_f32_e32 v5, v156, v157
	v_add_f32_e32 v6, v6, v7
	v_sub_f32_e32 v7, v152, v153
	v_add_f32_e32 v8, v8, v9
	v_sub_f32_e32 v9, v150, v151
	v_add_f32_e32 v10, v10, v11
	v_mul_f32_e32 v11, s88, v19
	v_mul_f32_e32 v19, s88, v22
	v_mul_f32_e32 v20, s88, v20
	v_mul_f32_e32 v21, s88, v21
	v_mul_f32_e32 v22, s88, v23
	v_mul_f32_e32 v23, s88, v24
	v_mul_f32_e32 v24, s88, v25
	v_mul_f32_e32 v25, s88, v26
	v_mul_f32_e32 v26, s88, v27
	v_mul_f32_e32 v27, s88, v4
	v_mul_f32_e32 v28, s88, v5
	v_cvt_pk_bf16_f32 v4, v11, v19
	v_cvt_pk_bf16_f32 v5, v20, v21
	v_mul_f32_e32 v29, s88, v6
	v_mul_f32_e32 v30, s88, v7
	v_mul_f32_e32 v8, s88, v8
	v_mul_f32_e32 v9, s88, v9
	v_mul_f32_e32 v10, s88, v10
	v_cvt_pk_bf16_f32 v6, v22, v23
	v_cvt_pk_bf16_f32 v7, v24, v25
	global_store_dwordx4 v[2:3], v[4:7], off
	v_cvt_pk_bf16_f32 v2, v26, v27
	v_cvt_pk_bf16_f32 v3, v28, v29
	s_nop 1
	v_cvt_pk_bf16_f32 v4, v30, v8
	v_cvt_pk_bf16_f32 v5, v9, v10
	global_store_dwordx4 v[12:13], v[2:5], off
	s_nop 1
	v_mov_b64_e32 v[2:3], v[190:191]
	v_mov_b64_e32 v[4:5], v[192:193]
	s_nop 0
	v_mov_b64_e32 v[6:7], v[194:195]
	v_mov_b64_e32 v[8:9], v[196:197]
	v_lshlrev_b64 v[12:13], 8, v[14:15]
	v_lshl_add_u64 v[12:13], s[46:47], 0, v[12:13]
	v_lshl_add_u64 v[12:13], v[12:13], 0, s[16:17]
	v_add_u32_e32 v10, 32, v18
	v_lshl_add_u64 v[12:13], v[12:13], 0, v[174:175]
	v_ashrrev_i32_e32 v11, 31, v10
	v_add_co_u32_e32 v16, vcc, s77, v12
	v_lshlrev_b64 v[14:15], 9, v[10:11]
	s_nop 0
	v_addc_co_u32_e32 v17, vcc, 0, v13, vcc
	v_lshl_add_u64 v[14:15], v[178:179], 0, v[14:15]
	v_lshlrev_b64 v[10:11], 8, v[10:11]
	v_lshl_add_u64 v[10:11], s[46:47], 0, v[10:11]
	v_lshl_add_u64 v[10:11], v[10:11], 0, s[16:17]
	v_lshl_add_u64 v[10:11], v[10:11], 0, v[174:175]
	v_pk_mul_f32 v[20:21], v[144:145], v[4:5]
	v_pk_mul_f32 v[22:23], v[142:143], v[2:3]
	v_pk_mul_f32 v[24:25], v[142:143], v[2:3] op_sel:[1,0] op_sel_hi:[0,1]
	v_pk_mul_f32 v[26:27], v[144:145], v[4:5] op_sel:[1,0] op_sel_hi:[0,1]
	v_pk_mul_f32 v[28:29], v[140:141], v[8:9]
	v_pk_mul_f32 v[30:31], v[138:139], v[6:7]
	v_pk_mul_f32 v[32:33], v[138:139], v[6:7] op_sel:[1,0] op_sel_hi:[0,1]
	v_pk_mul_f32 v[138:139], v[140:141], v[8:9] op_sel:[1,0] op_sel_hi:[0,1]
	v_pk_mul_f32 v[140:141], v[136:137], v[4:5]
	v_pk_mul_f32 v[142:143], v[134:135], v[2:3]
	v_pk_mul_f32 v[2:3], v[134:135], v[2:3] op_sel:[1,0] op_sel_hi:[0,1]
	v_pk_mul_f32 v[4:5], v[136:137], v[4:5] op_sel:[1,0] op_sel_hi:[0,1]
	v_pk_mul_f32 v[136:137], v[130:131], v[6:7]
	v_pk_mul_f32 v[134:135], v[132:133], v[8:9]
	v_pk_mul_f32 v[6:7], v[130:131], v[6:7] op_sel:[1,0] op_sel_hi:[0,1]
	v_pk_mul_f32 v[8:9], v[132:133], v[8:9] op_sel:[1,0] op_sel_hi:[0,1]
	v_sub_f32_e32 v19, v22, v23
	v_add_f32_e32 v22, v24, v25
	v_sub_f32_e32 v20, v20, v21
	v_add_f32_e32 v21, v26, v27
	v_sub_f32_e32 v23, v30, v31
	v_add_f32_e32 v24, v32, v33
	v_sub_f32_e32 v25, v28, v29
	v_add_f32_e32 v26, v138, v139
	v_sub_f32_e32 v27, v142, v143
	v_add_f32_e32 v2, v2, v3
	v_sub_f32_e32 v3, v140, v141
	v_add_f32_e32 v4, v4, v5
	v_sub_f32_e32 v5, v136, v137
	v_add_f32_e32 v6, v6, v7
; #define GAS __attribute__((address_space(1)))
; __device__ __forceinline__ unsigned cvt_pk_bf16(float lo, float hi) { unsigned r; asm volatile("v_cvt_pk_bf16_f32 %0, %1, %2" : "=v"(r) : "v"(lo), "v"(hi)); return r; }
;     __device__ __forceinline__ bool operator()(f32x4 (&acc)[2][2][4][2], const Unit& u, int wr, int wc, int fr, int fq, LAS unsigned char* scr) const {
;     ...
;                 for (int m = 0; m < 4; ++m) { const int row = row0 + ai * 128 + m * 16; GAS bf16_t* rowp = H + HOFF(colt, row) + cl;
;                     const f32x4 cs0 = rope[(size_t)row * 32 + (i0 >> 1)], cs1 = rope[(size_t)row * 32 + (i0 >> 1) + 1];
; #pragma unroll
;                     for (int bj = 0; bj < 2; ++bj) { const f32x4 v0 = acc[ai][bj][m][0], v1 = acc[ai][bj][m][1]; u32x4 w;
;                         w.x = cvt_pk_bf16((v0[0] * cs0[0] - v0[1] * cs0[1]) * sc, (v0[1] * cs0[0] + v0[0] * cs0[1]) * sc);
;                         w.y = cvt_pk_bf16((v0[2] * cs0[2] - v0[3] * cs0[3]) * sc, (v0[3] * cs0[2] + v0[2] * cs0[3]) * sc);
;                         w.z = cvt_pk_bf16((v1[0] * cs1[0] - v1[1] * cs1[1]) * sc, (v1[1] * cs1[0] + v1[0] * cs1[1]) * sc);
;                         w.w = cvt_pk_bf16((v1[2] * cs1[2] - v1[3] * cs1[3]) * sc, (v1[3] * cs1[2] + v1[2] * cs1[3]) * sc);
;                         *(GAS u32x4*)(rowp + (size_t)bj * T * 128) = w; } }
	v_sub_f32_e32 v7, v134, v135
	v_add_f32_e32 v8, v8, v9
	v_mul_f32_e32 v9, s88, v19
	v_mul_f32_e32 v19, s88, v22
	v_mul_f32_e32 v20, s88, v20
	v_mul_f32_e32 v21, s88, v21
	v_mul_f32_e32 v22, s88, v23
	v_mul_f32_e32 v23, s88, v24
	v_mul_f32_e32 v24, s88, v25
	v_mul_f32_e32 v25, s88, v26
	v_mul_f32_e32 v26, s88, v27
	v_mul_f32_e32 v27, s88, v2
	v_mul_f32_e32 v28, s88, v3
	v_mul_f32_e32 v29, s88, v4
	v_mul_f32_e32 v30, s88, v5
	v_cvt_pk_bf16_f32 v2, v9, v19
	v_cvt_pk_bf16_f32 v3, v20, v21
	v_cvt_pk_bf16_f32 v4, v22, v23
	v_cvt_pk_bf16_f32 v5, v24, v25
	v_mul_f32_e32 v6, s88, v6
	v_mul_f32_e32 v7, s88, v7
	v_mul_f32_e32 v8, s88, v8
	global_store_dwordx4 v[12:13], v[2:5], off
	v_add_u32_e32 v12, 48, v18
	v_ashrrev_i32_e32 v13, 31, v12
	v_cvt_pk_bf16_f32 v2, v26, v27
	v_cvt_pk_bf16_f32 v3, v28, v29
	v_cvt_pk_bf16_f32 v4, v30, v6
	v_cvt_pk_bf16_f32 v5, v7, v8
	global_store_dwordx4 v[16:17], v[2:5], off
	s_nop 1
	v_mov_b64_e32 v[2:3], v[210:211]
	v_mov_b64_e32 v[4:5], v[212:213]
	s_nop 0
	v_mov_b64_e32 v[6:7], v[214:215]
	v_mov_b64_e32 v[8:9], v[216:217]
	v_add_co_u32_e32 v16, vcc, s77, v10
	v_lshlrev_b64 v[14:15], 9, v[12:13]
	s_nop 0
	v_addc_co_u32_e32 v17, vcc, 0, v11, vcc
	v_lshl_add_u64 v[14:15], v[178:179], 0, v[14:15]
	v_lshlrev_b64 v[12:13], 8, v[12:13]
	v_lshl_add_u64 v[12:13], s[46:47], 0, v[12:13]
	v_lshl_add_u64 v[12:13], v[12:13], 0, s[16:17]
	v_lshl_add_u64 v[12:13], v[12:13], 0, v[174:175]
	v_pk_mul_f32 v[20:21], v[128:129], v[4:5]
	v_pk_mul_f32 v[22:23], v[126:127], v[2:3]
	v_pk_mul_f32 v[24:25], v[126:127], v[2:3] op_sel:[1,0] op_sel_hi:[0,1]
	v_pk_mul_f32 v[26:27], v[128:129], v[4:5] op_sel:[1,0] op_sel_hi:[0,1]
	v_pk_mul_f32 v[28:29], v[124:125], v[8:9]
	v_pk_mul_f32 v[30:31], v[122:123], v[6:7]
	v_pk_mul_f32 v[32:33], v[122:123], v[6:7] op_sel:[1,0] op_sel_hi:[0,1]
	v_pk_mul_f32 v[122:123], v[124:125], v[8:9] op_sel:[1,0] op_sel_hi:[0,1]
	v_pk_mul_f32 v[124:125], v[120:121], v[4:5]
	v_pk_mul_f32 v[126:127], v[118:119], v[2:3]
	v_pk_mul_f32 v[2:3], v[118:119], v[2:3] op_sel:[1,0] op_sel_hi:[0,1]
	v_pk_mul_f32 v[4:5], v[120:121], v[4:5] op_sel:[1,0] op_sel_hi:[0,1]
	v_pk_mul_f32 v[120:121], v[114:115], v[6:7]
	v_pk_mul_f32 v[118:119], v[116:117], v[8:9]
	v_pk_mul_f32 v[6:7], v[114:115], v[6:7] op_sel:[1,0] op_sel_hi:[0,1]
	v_pk_mul_f32 v[8:9], v[116:117], v[8:9] op_sel:[1,0] op_sel_hi:[0,1]
	v_sub_f32_e32 v19, v22, v23
	v_add_f32_e32 v22, v24, v25
	v_sub_f32_e32 v20, v20, v21
	v_add_f32_e32 v21, v26, v27
	v_sub_f32_e32 v23, v30, v31
	v_add_f32_e32 v24, v32, v33
	v_sub_f32_e32 v25, v28, v29
	v_add_f32_e32 v26, v122, v123
	v_sub_f32_e32 v27, v126, v127
	v_add_f32_e32 v2, v2, v3
	v_sub_f32_e32 v3, v124, v125
	v_add_f32_e32 v4, v4, v5
	v_sub_f32_e32 v5, v120, v121
	v_add_f32_e32 v6, v6, v7
	v_sub_f32_e32 v7, v118, v119
	v_add_f32_e32 v8, v8, v9
	v_mul_f32_e32 v9, s88, v19
	v_mul_f32_e32 v19, s88, v22
	v_mul_f32_e32 v20, s88, v20
	v_mul_f32_e32 v21, s88, v21
	v_mul_f32_e32 v22, s88, v23
	v_mul_f32_e32 v23, s88, v24
	v_mul_f32_e32 v24, s88, v25
	v_mul_f32_e32 v25, s88, v26
	v_mul_f32_e32 v26, s88, v27
	v_mul_f32_e32 v27, s88, v2
	v_mul_f32_e32 v28, s88, v3
	v_mul_f32_e32 v29, s88, v4
	v_mul_f32_e32 v30, s88, v5
	v_cvt_pk_bf16_f32 v2, v9, v19
	v_cvt_pk_bf16_f32 v3, v20, v21
	v_cvt_pk_bf16_f32 v4, v22, v23
	v_cvt_pk_bf16_f32 v5, v24, v25
	v_mul_f32_e32 v6, s88, v6
	v_mul_f32_e32 v7, s88, v7
	v_mul_f32_e32 v8, s88, v8
	global_store_dwordx4 v[10:11], v[2:5], off
	v_add_u32_e32 v10, 0x80, v18
	v_ashrrev_i32_e32 v11, 31, v10
	v_cvt_pk_bf16_f32 v2, v26, v27
	v_cvt_pk_bf16_f32 v3, v28, v29
	v_cvt_pk_bf16_f32 v4, v30, v6
	v_cvt_pk_bf16_f32 v5, v7, v8
	global_store_dwordx4 v[16:17], v[2:5], off
	s_nop 1
	v_mov_b64_e32 v[2:3], v[218:219]
	v_mov_b64_e32 v[4:5], v[220:221]
	s_nop 0
	v_mov_b64_e32 v[6:7], v[222:223]
	v_mov_b64_e32 v[8:9], v[224:225]
	v_add_co_u32_e32 v16, vcc, s77, v12
	v_lshlrev_b64 v[14:15], 9, v[10:11]
	s_nop 0
	v_addc_co_u32_e32 v17, vcc, 0, v13, vcc
	v_lshl_add_u64 v[14:15], v[178:179], 0, v[14:15]
	v_lshlrev_b64 v[10:11], 8, v[10:11]
	v_lshl_add_u64 v[10:11], s[46:47], 0, v[10:11]
	v_lshl_add_u64 v[10:11], v[10:11], 0, s[16:17]
	v_lshl_add_u64 v[10:11], v[10:11], 0, v[174:175]
	v_pk_mul_f32 v[20:21], v[112:113], v[4:5]
	v_pk_mul_f32 v[22:23], v[110:111], v[2:3]
	v_pk_mul_f32 v[24:25], v[110:111], v[2:3] op_sel:[1,0] op_sel_hi:[0,1]
	v_pk_mul_f32 v[26:27], v[112:113], v[4:5] op_sel:[1,0] op_sel_hi:[0,1]
	v_pk_mul_f32 v[28:29], v[108:109], v[8:9]
	v_pk_mul_f32 v[30:31], v[106:107], v[6:7]
	v_pk_mul_f32 v[32:33], v[106:107], v[6:7] op_sel:[1,0] op_sel_hi:[0,1]
	v_pk_mul_f32 v[106:107], v[108:109], v[8:9] op_sel:[1,0] op_sel_hi:[0,1]
	v_pk_mul_f32 v[108:109], v[104:105], v[4:5]
	v_pk_mul_f32 v[110:111], v[102:103], v[2:3]
	v_pk_mul_f32 v[2:3], v[102:103], v[2:3] op_sel:[1,0] op_sel_hi:[0,1]
	v_pk_mul_f32 v[4:5], v[104:105], v[4:5] op_sel:[1,0] op_sel_hi:[0,1]
	v_pk_mul_f32 v[104:105], v[98:99], v[6:7]
	v_pk_mul_f32 v[102:103], v[100:101], v[8:9]
	v_pk_mul_f32 v[6:7], v[98:99], v[6:7] op_sel:[1,0] op_sel_hi:[0,1]
	v_pk_mul_f32 v[8:9], v[100:101], v[8:9] op_sel:[1,0] op_sel_hi:[0,1]
	v_sub_f32_e32 v19, v22, v23
	v_add_f32_e32 v22, v24, v25
	v_sub_f32_e32 v20, v20, v21
	v_add_f32_e32 v21, v26, v27
	v_sub_f32_e32 v23, v30, v31
	v_add_f32_e32 v24, v32, v33
	v_sub_f32_e32 v25, v28, v29
	v_add_f32_e32 v26, v106, v107
	v_sub_f32_e32 v27, v110, v111
	v_add_f32_e32 v2, v2, v3
	v_sub_f32_e32 v3, v108, v109
	v_add_f32_e32 v4, v4, v5
	v_sub_f32_e32 v5, v104, v105
	v_add_f32_e32 v6, v6, v7
	v_sub_f32_e32 v7, v102, v103
	v_add_f32_e32 v8, v8, v9
	v_mul_f32_e32 v9, s88, v19
	v_mul_f32_e32 v19, s88, v22
	v_mul_f32_e32 v20, s88, v20
; #define GAS __attribute__((address_space(1)))
; __device__ __forceinline__ unsigned cvt_pk_bf16(float lo, float hi) { unsigned r; asm volatile("v_cvt_pk_bf16_f32 %0, %1, %2" : "=v"(r) : "v"(lo), "v"(hi)); return r; }
;     __device__ __forceinline__ bool operator()(f32x4 (&acc)[2][2][4][2], const Unit& u, int wr, int wc, int fr, int fq, LAS unsigned char* scr) const {
;     ...
;                 for (int m = 0; m < 4; ++m) { const int row = row0 + ai * 128 + m * 16; GAS bf16_t* rowp = H + HOFF(colt, row) + cl;
;                     const f32x4 cs0 = rope[(size_t)row * 32 + (i0 >> 1)], cs1 = rope[(size_t)row * 32 + (i0 >> 1) + 1];
; #pragma unroll
;                     for (int bj = 0; bj < 2; ++bj) { const f32x4 v0 = acc[ai][bj][m][0], v1 = acc[ai][bj][m][1]; u32x4 w;
;                         w.x = cvt_pk_bf16((v0[0] * cs0[0] - v0[1] * cs0[1]) * sc, (v0[1] * cs0[0] + v0[0] * cs0[1]) * sc);
;                         w.y = cvt_pk_bf16((v0[2] * cs0[2] - v0[3] * cs0[3]) * sc, (v0[3] * cs0[2] + v0[2] * cs0[3]) * sc);
;                         w.z = cvt_pk_bf16((v1[0] * cs1[0] - v1[1] * cs1[1]) * sc, (v1[1] * cs1[0] + v1[0] * cs1[1]) * sc);
;                         w.w = cvt_pk_bf16((v1[2] * cs1[2] - v1[3] * cs1[3]) * sc, (v1[3] * cs1[2] + v1[2] * cs1[3]) * sc);
;                         *(GAS u32x4*)(rowp + (size_t)bj * T * 128) = w; } }
	v_mul_f32_e32 v21, s88, v21
	v_mul_f32_e32 v22, s88, v23
	v_mul_f32_e32 v23, s88, v24
	v_mul_f32_e32 v24, s88, v25
	v_mul_f32_e32 v25, s88, v26
	v_mul_f32_e32 v26, s88, v27
	v_mul_f32_e32 v27, s88, v2
	v_mul_f32_e32 v28, s88, v3
	v_mul_f32_e32 v29, s88, v4
	v_mul_f32_e32 v30, s88, v5
	v_cvt_pk_bf16_f32 v2, v9, v19
	v_cvt_pk_bf16_f32 v3, v20, v21
	v_cvt_pk_bf16_f32 v4, v22, v23
	v_cvt_pk_bf16_f32 v5, v24, v25
	v_mul_f32_e32 v6, s88, v6
	v_mul_f32_e32 v7, s88, v7
	v_mul_f32_e32 v8, s88, v8
	global_store_dwordx4 v[12:13], v[2:5], off
	v_add_u32_e32 v12, 0x90, v18
	v_ashrrev_i32_e32 v13, 31, v12
	v_cvt_pk_bf16_f32 v2, v26, v27
	v_cvt_pk_bf16_f32 v3, v28, v29
	v_cvt_pk_bf16_f32 v4, v30, v6
	v_cvt_pk_bf16_f32 v5, v7, v8
	global_store_dwordx4 v[16:17], v[2:5], off
	s_nop 1
	v_mov_b64_e32 v[2:3], v[226:227]
	v_mov_b64_e32 v[4:5], v[228:229]
	s_nop 0
	v_mov_b64_e32 v[6:7], v[230:231]
	v_mov_b64_e32 v[8:9], v[232:233]
	v_add_co_u32_e32 v16, vcc, s77, v10
	v_lshlrev_b64 v[14:15], 9, v[12:13]
	s_nop 0
	v_addc_co_u32_e32 v17, vcc, 0, v11, vcc
	v_lshl_add_u64 v[14:15], v[178:179], 0, v[14:15]
	v_lshlrev_b64 v[12:13], 8, v[12:13]
	v_lshl_add_u64 v[12:13], s[46:47], 0, v[12:13]
	v_lshl_add_u64 v[12:13], v[12:13], 0, s[16:17]
	v_lshl_add_u64 v[12:13], v[12:13], 0, v[174:175]
	v_pk_mul_f32 v[20:21], v[88:89], v[4:5]
	v_pk_mul_f32 v[22:23], v[86:87], v[2:3]
	v_pk_mul_f32 v[24:25], v[86:87], v[2:3] op_sel:[1,0] op_sel_hi:[0,1]
	v_pk_mul_f32 v[26:27], v[88:89], v[4:5] op_sel:[1,0] op_sel_hi:[0,1]
	v_pk_mul_f32 v[28:29], v[84:85], v[8:9]
	v_pk_mul_f32 v[30:31], v[82:83], v[6:7]
	v_pk_mul_f32 v[32:33], v[82:83], v[6:7] op_sel:[1,0] op_sel_hi:[0,1]
	v_pk_mul_f32 v[82:83], v[84:85], v[8:9] op_sel:[1,0] op_sel_hi:[0,1]
	v_pk_mul_f32 v[84:85], v[96:97], v[4:5]
	v_pk_mul_f32 v[86:87], v[94:95], v[2:3]
	v_pk_mul_f32 v[2:3], v[94:95], v[2:3] op_sel:[1,0] op_sel_hi:[0,1]
	v_pk_mul_f32 v[4:5], v[96:97], v[4:5] op_sel:[1,0] op_sel_hi:[0,1]
	v_pk_mul_f32 v[94:95], v[90:91], v[6:7]
	v_pk_mul_f32 v[88:89], v[92:93], v[8:9]
	v_pk_mul_f32 v[6:7], v[90:91], v[6:7] op_sel:[1,0] op_sel_hi:[0,1]
	v_pk_mul_f32 v[8:9], v[92:93], v[8:9] op_sel:[1,0] op_sel_hi:[0,1]
	v_sub_f32_e32 v19, v22, v23
	v_add_f32_e32 v22, v24, v25
	v_sub_f32_e32 v20, v20, v21
	v_add_f32_e32 v21, v26, v27
	v_sub_f32_e32 v23, v30, v31
	v_add_f32_e32 v24, v32, v33
	v_sub_f32_e32 v25, v28, v29
	v_add_f32_e32 v26, v82, v83
	v_sub_f32_e32 v27, v86, v87
	v_add_f32_e32 v2, v2, v3
	v_sub_f32_e32 v3, v84, v85
	v_add_f32_e32 v4, v4, v5
	v_sub_f32_e32 v5, v94, v95
	v_add_f32_e32 v6, v6, v7
	v_sub_f32_e32 v7, v88, v89
	v_add_f32_e32 v8, v8, v9
	v_mul_f32_e32 v9, s88, v19
	v_mul_f32_e32 v19, s88, v22
	v_mul_f32_e32 v20, s88, v20
	v_mul_f32_e32 v21, s88, v21
	v_mul_f32_e32 v22, s88, v23
	v_mul_f32_e32 v23, s88, v24
	v_mul_f32_e32 v24, s88, v25
	v_mul_f32_e32 v25, s88, v26
	v_mul_f32_e32 v26, s88, v27
	v_mul_f32_e32 v27, s88, v2
	v_mul_f32_e32 v28, s88, v3
	v_mul_f32_e32 v29, s88, v4
	v_mul_f32_e32 v30, s88, v5
	v_cvt_pk_bf16_f32 v2, v9, v19
	v_cvt_pk_bf16_f32 v3, v20, v21
	v_cvt_pk_bf16_f32 v4, v22, v23
	v_cvt_pk_bf16_f32 v5, v24, v25
	v_mul_f32_e32 v6, s88, v6
	v_mul_f32_e32 v7, s88, v7
	v_mul_f32_e32 v8, s88, v8
	global_store_dwordx4 v[10:11], v[2:5], off
	v_add_u32_e32 v10, 0xa0, v18
	v_ashrrev_i32_e32 v11, 31, v10
	v_cvt_pk_bf16_f32 v2, v26, v27
	v_cvt_pk_bf16_f32 v3, v28, v29
	v_cvt_pk_bf16_f32 v4, v30, v6
	v_cvt_pk_bf16_f32 v5, v7, v8
	global_store_dwordx4 v[16:17], v[2:5], off
	s_nop 1
	v_mov_b64_e32 v[2:3], v[234:235]
	v_mov_b64_e32 v[4:5], v[236:237]
	s_nop 0
	v_mov_b64_e32 v[6:7], v[238:239]
	v_mov_b64_e32 v[8:9], v[240:241]
	v_add_co_u32_e32 v16, vcc, s77, v12
	v_lshlrev_b64 v[14:15], 9, v[10:11]
	s_nop 0
	v_addc_co_u32_e32 v17, vcc, 0, v13, vcc
	v_lshl_add_u64 v[14:15], v[178:179], 0, v[14:15]
	v_lshlrev_b64 v[10:11], 8, v[10:11]
	v_lshl_add_u64 v[10:11], s[46:47], 0, v[10:11]
	v_lshl_add_u64 v[10:11], v[10:11], 0, s[16:17]
	v_lshl_add_u64 v[10:11], v[10:11], 0, v[174:175]
	v_pk_mul_f32 v[20:21], v[72:73], v[4:5]
	v_pk_mul_f32 v[22:23], v[70:71], v[2:3]
	v_pk_mul_f32 v[24:25], v[70:71], v[2:3] op_sel:[1,0] op_sel_hi:[0,1]
	v_pk_mul_f32 v[26:27], v[72:73], v[4:5] op_sel:[1,0] op_sel_hi:[0,1]
	v_pk_mul_f32 v[28:29], v[68:69], v[8:9]
	v_pk_mul_f32 v[30:31], v[66:67], v[6:7]
	v_pk_mul_f32 v[32:33], v[66:67], v[6:7] op_sel:[1,0] op_sel_hi:[0,1]
	v_pk_mul_f32 v[66:67], v[68:69], v[8:9] op_sel:[1,0] op_sel_hi:[0,1]
	v_pk_mul_f32 v[68:69], v[80:81], v[4:5]
	v_pk_mul_f32 v[70:71], v[78:79], v[2:3]
	v_pk_mul_f32 v[2:3], v[78:79], v[2:3] op_sel:[1,0] op_sel_hi:[0,1]
	v_pk_mul_f32 v[4:5], v[80:81], v[4:5] op_sel:[1,0] op_sel_hi:[0,1]
	v_pk_mul_f32 v[78:79], v[74:75], v[6:7]
	v_pk_mul_f32 v[72:73], v[76:77], v[8:9]
	v_pk_mul_f32 v[6:7], v[74:75], v[6:7] op_sel:[1,0] op_sel_hi:[0,1]
	v_pk_mul_f32 v[8:9], v[76:77], v[8:9] op_sel:[1,0] op_sel_hi:[0,1]
	v_sub_f32_e32 v19, v22, v23
	v_add_f32_e32 v22, v24, v25
	v_sub_f32_e32 v20, v20, v21
	v_add_f32_e32 v21, v26, v27
	v_sub_f32_e32 v23, v30, v31
	v_add_f32_e32 v24, v32, v33
	v_sub_f32_e32 v25, v28, v29
	v_add_f32_e32 v26, v66, v67
	v_sub_f32_e32 v27, v70, v71
	v_add_f32_e32 v2, v2, v3
	v_sub_f32_e32 v3, v68, v69
	v_add_f32_e32 v4, v4, v5
	v_sub_f32_e32 v5, v78, v79
	v_add_f32_e32 v6, v6, v7
	v_sub_f32_e32 v7, v72, v73
	v_add_f32_e32 v8, v8, v9
	v_mul_f32_e32 v9, s88, v19
	v_mul_f32_e32 v19, s88, v22
	v_mul_f32_e32 v20, s88, v20
	v_mul_f32_e32 v21, s88, v21
	v_mul_f32_e32 v22, s88, v23
	v_mul_f32_e32 v23, s88, v24
	v_mul_f32_e32 v24, s88, v25
	v_mul_f32_e32 v25, s88, v26
	v_mul_f32_e32 v26, s88, v27
	v_mul_f32_e32 v27, s88, v2
	v_mul_f32_e32 v28, s88, v3
	v_mul_f32_e32 v29, s88, v4
	v_mul_f32_e32 v30, s88, v5
	v_cvt_pk_bf16_f32 v2, v9, v19
	v_cvt_pk_bf16_f32 v3, v20, v21
	v_cvt_pk_bf16_f32 v4, v22, v23
	v_cvt_pk_bf16_f32 v5, v24, v25
	v_mul_f32_e32 v6, s88, v6
	v_mul_f32_e32 v7, s88, v7
	v_mul_f32_e32 v8, s88, v8
	global_store_dwordx4 v[12:13], v[2:5], off
	v_add_u32_e32 v12, 0xb0, v18
	v_ashrrev_i32_e32 v13, 31, v12
	v_cvt_pk_bf16_f32 v2, v26, v27
	v_cvt_pk_bf16_f32 v3, v28, v29
	v_cvt_pk_bf16_f32 v4, v30, v6
	v_cvt_pk_bf16_f32 v5, v7, v8
	global_store_dwordx4 v[16:17], v[2:5], off
	global_load_dwordx4 v[2:5], v[14:15], off
	s_nop 0
	global_load_dwordx4 v[6:9], v[14:15], off offset:16
	v_add_co_u32_e32 v16, vcc, s77, v10
	v_lshlrev_b64 v[14:15], 9, v[12:13]
	s_nop 0
	v_addc_co_u32_e32 v17, vcc, 0, v11, vcc
	v_lshl_add_u64 v[14:15], v[178:179], 0, v[14:15]
	s_waitcnt vmcnt(1)
; #define GAS __attribute__((address_space(1)))
; __device__ __forceinline__ unsigned cvt_pk_bf16(float lo, float hi) { unsigned r; asm volatile("v_cvt_pk_bf16_f32 %0, %1, %2" : "=v"(r) : "v"(lo), "v"(hi)); return r; }
;     __device__ __forceinline__ bool operator()(f32x4 (&acc)[2][2][4][2], const Unit& u, int wr, int wc, int fr, int fq, LAS unsigned char* scr) const {
;     ...
;             for (int ai = 0; ai < 2; ++ai)
; #pragma unroll
;                 for (int m = 0; m < 4; ++m) { const int row = row0 + ai * 128 + m * 16; GAS bf16_t* rowp = H + HOFF(colt, row) + cl;
;                     const f32x4 cs0 = rope[(size_t)row * 32 + (i0 >> 1)], cs1 = rope[(size_t)row * 32 + (i0 >> 1) + 1];
; #pragma unroll
;                     for (int bj = 0; bj < 2; ++bj) { const f32x4 v0 = acc[ai][bj][m][0], v1 = acc[ai][bj][m][1]; u32x4 w;
;                         w.x = cvt_pk_bf16((v0[0] * cs0[0] - v0[1] * cs0[1]) * sc, (v0[1] * cs0[0] + v0[0] * cs0[1]) * sc);
;                         w.y = cvt_pk_bf16((v0[2] * cs0[2] - v0[3] * cs0[3]) * sc, (v0[3] * cs0[2] + v0[2] * cs0[3]) * sc);
;                         w.z = cvt_pk_bf16((v1[0] * cs1[0] - v1[1] * cs1[1]) * sc, (v1[1] * cs1[0] + v1[0] * cs1[1]) * sc);
;                         w.w = cvt_pk_bf16((v1[2] * cs1[2] - v1[3] * cs1[3]) * sc, (v1[3] * cs1[2] + v1[2] * cs1[3]) * sc);
;                         *(GAS u32x4*)(rowp + (size_t)bj * T * 128) = w; } }
	v_pk_mul_f32 v[18:19], v[56:57], v[4:5]
	v_pk_mul_f32 v[20:21], v[54:55], v[2:3]
	v_pk_mul_f32 v[22:23], v[54:55], v[2:3] op_sel:[1,0] op_sel_hi:[0,1]
	v_pk_mul_f32 v[24:25], v[56:57], v[4:5] op_sel:[1,0] op_sel_hi:[0,1]
	s_waitcnt vmcnt(0)
	v_pk_mul_f32 v[26:27], v[52:53], v[8:9]
	v_pk_mul_f32 v[28:29], v[50:51], v[6:7]
	v_pk_mul_f32 v[30:31], v[50:51], v[6:7] op_sel:[1,0] op_sel_hi:[0,1]
	v_pk_mul_f32 v[32:33], v[52:53], v[8:9] op_sel:[1,0] op_sel_hi:[0,1]
	v_pk_mul_f32 v[50:51], v[64:65], v[4:5]
	v_pk_mul_f32 v[52:53], v[62:63], v[2:3]
	v_pk_mul_f32 v[2:3], v[62:63], v[2:3] op_sel:[1,0] op_sel_hi:[0,1]
	v_pk_mul_f32 v[4:5], v[64:65], v[4:5] op_sel:[1,0] op_sel_hi:[0,1]
	v_pk_mul_f32 v[56:57], v[58:59], v[6:7]
	v_pk_mul_f32 v[54:55], v[60:61], v[8:9]
	v_pk_mul_f32 v[6:7], v[58:59], v[6:7] op_sel:[1,0] op_sel_hi:[0,1]
	v_pk_mul_f32 v[8:9], v[60:61], v[8:9] op_sel:[1,0] op_sel_hi:[0,1]
	v_sub_f32_e32 v20, v20, v21
	v_add_f32_e32 v21, v22, v23
	v_sub_f32_e32 v18, v18, v19
	v_add_f32_e32 v19, v24, v25
	v_sub_f32_e32 v22, v28, v29
	v_add_f32_e32 v23, v30, v31
	v_sub_f32_e32 v24, v26, v27
	v_add_f32_e32 v25, v32, v33
	v_sub_f32_e32 v26, v52, v53
	v_add_f32_e32 v2, v2, v3
	v_sub_f32_e32 v3, v50, v51
	v_add_f32_e32 v4, v4, v5
	v_sub_f32_e32 v5, v56, v57
	v_add_f32_e32 v6, v6, v7
	v_sub_f32_e32 v7, v54, v55
	v_add_f32_e32 v8, v8, v9
	v_mul_f32_e32 v9, s88, v20
	v_mul_f32_e32 v20, s88, v21
	v_mul_f32_e32 v18, s88, v18
	v_mul_f32_e32 v19, s88, v19
	v_mul_f32_e32 v21, s88, v22
	v_mul_f32_e32 v22, s88, v23
	v_mul_f32_e32 v23, s88, v24
	v_mul_f32_e32 v24, s88, v25
	v_mul_f32_e32 v25, s88, v26
	v_mul_f32_e32 v26, s88, v2
	v_mul_f32_e32 v27, s88, v3
	v_mul_f32_e32 v28, s88, v4
	v_mul_f32_e32 v29, s88, v5
	v_cvt_pk_bf16_f32 v2, v9, v20
	v_cvt_pk_bf16_f32 v3, v18, v19
	v_cvt_pk_bf16_f32 v4, v21, v22
	v_cvt_pk_bf16_f32 v5, v23, v24
	v_mul_f32_e32 v6, s88, v6
	v_mul_f32_e32 v7, s88, v7
	v_mul_f32_e32 v8, s88, v8
	global_store_dwordx4 v[10:11], v[2:5], off
	v_lshlrev_b64 v[10:11], 8, v[12:13]
	v_lshl_add_u64 v[10:11], s[46:47], 0, v[10:11]
	v_cvt_pk_bf16_f32 v2, v25, v26
	v_cvt_pk_bf16_f32 v3, v27, v28
	v_cvt_pk_bf16_f32 v4, v29, v6
	v_cvt_pk_bf16_f32 v5, v7, v8
	global_store_dwordx4 v[16:17], v[2:5], off
	global_load_dwordx4 v[2:5], v[14:15], off
	s_nop 0
	global_load_dwordx4 v[6:9], v[14:15], off offset:16
	v_lshl_add_u64 v[10:11], v[10:11], 0, s[16:17]
	v_lshl_add_u64 v[10:11], v[10:11], 0, v[174:175]
	v_add_co_u32_e32 v12, vcc, 0x400000, v10
	s_waitcnt vmcnt(1)
	v_pk_mul_f32 v[16:17], v[38:39], v[2:3]
	v_pk_mul_f32 v[18:19], v[38:39], v[2:3] op_sel:[1,0] op_sel_hi:[0,1]
	v_pk_mul_f32 v[14:15], v[40:41], v[4:5]
	v_pk_mul_f32 v[20:21], v[40:41], v[4:5] op_sel:[1,0] op_sel_hi:[0,1]
	s_waitcnt vmcnt(0)
	v_pk_mul_f32 v[22:23], v[36:37], v[8:9]
	v_pk_mul_f32 v[24:25], v[34:35], v[6:7]
	v_pk_mul_f32 v[26:27], v[34:35], v[6:7] op_sel:[1,0] op_sel_hi:[0,1]
	v_pk_mul_f32 v[28:29], v[36:37], v[8:9] op_sel:[1,0] op_sel_hi:[0,1]
	v_pk_mul_f32 v[30:31], v[48:49], v[4:5]
	v_pk_mul_f32 v[32:33], v[46:47], v[2:3]
	v_pk_mul_f32 v[2:3], v[46:47], v[2:3] op_sel:[1,0] op_sel_hi:[0,1]
	v_pk_mul_f32 v[4:5], v[48:49], v[4:5] op_sel:[1,0] op_sel_hi:[0,1]
	v_pk_mul_f32 v[34:35], v[44:45], v[8:9]
	v_pk_mul_f32 v[36:37], v[42:43], v[6:7]
	v_pk_mul_f32 v[8:9], v[44:45], v[8:9] op_sel:[1,0] op_sel_hi:[0,1]
	v_sub_f32_e32 v13, v16, v17
	v_add_f32_e32 v16, v18, v19
	v_pk_mul_f32 v[6:7], v[42:43], v[6:7] op_sel:[1,0] op_sel_hi:[0,1]
	v_sub_f32_e32 v14, v14, v15
	v_add_f32_e32 v15, v20, v21
	v_sub_f32_e32 v17, v24, v25
	v_add_f32_e32 v18, v26, v27
	v_sub_f32_e32 v19, v22, v23
	v_add_f32_e32 v20, v28, v29
	v_sub_f32_e32 v21, v32, v33
	v_add_f32_e32 v2, v2, v3
	v_sub_f32_e32 v3, v30, v31
	v_add_f32_e32 v4, v4, v5
	v_sub_f32_e32 v5, v36, v37
	v_add_f32_e32 v8, v8, v9
	v_mul_f32_e32 v9, s88, v13
	v_mul_f32_e32 v13, s88, v16
	v_add_f32_e32 v6, v6, v7
	v_sub_f32_e32 v7, v34, v35
	v_mul_f32_e32 v14, s88, v14
	v_mul_f32_e32 v15, s88, v15
	v_mul_f32_e32 v16, s88, v17
	v_mul_f32_e32 v17, s88, v18
	v_mul_f32_e32 v18, s88, v19
	v_mul_f32_e32 v19, s88, v20
	v_mul_f32_e32 v20, s88, v21
	v_mul_f32_e32 v21, s88, v2
	v_mul_f32_e32 v22, s88, v3
	v_mul_f32_e32 v23, s88, v4
	v_mul_f32_e32 v24, s88, v5
	v_cvt_pk_bf16_f32 v2, v9, v13
	v_cvt_pk_bf16_f32 v3, v14, v15
	v_cvt_pk_bf16_f32 v4, v16, v17
	v_cvt_pk_bf16_f32 v5, v18, v19
	v_addc_co_u32_e32 v13, vcc, 0, v11, vcc
	v_mul_f32_e32 v6, s88, v6
	v_mul_f32_e32 v7, s88, v7
	v_mul_f32_e32 v8, s88, v8
	global_store_dwordx4 v[10:11], v[2:5], off
	s_nop 1
	v_cvt_pk_bf16_f32 v2, v20, v21
	v_cvt_pk_bf16_f32 v3, v22, v23
	v_cvt_pk_bf16_f32 v4, v24, v6
	v_cvt_pk_bf16_f32 v5, v7, v8
	global_store_dwordx4 v[12:13], v[2:5], off
